# adds: P2 attention units issue the next queue pop when their tile loop ends (atomic round trip overlaps the unit tail; no lookahead across units)
# speedup vs baseline: 1.0017x; 1.0017x over previous
; __device__ __forceinline__ int otid() { int t = threadIdx.x; asm volatile("" : "+v"(t)); return t; }
; __device__ void phase2(const Params& p, unsigned char* smem, unsigned* qw) {
;     const int sub = otid() >> 8;
;     unsigned char* sm = smem + sub * ATT_SUB;
;     const int nchunks = 512, x = blockIdx.x & 7;
;     int* qslot = (int*)(smem + SM_PREF + 512);
;     bool conv_left = true, att_left = true;
;     int aq = 0;
;     const bool conv_first = blockIdx.x * 4 >= gridDim.x * 3;
.LBB0_369:
	v_writelane_b32 v248, s84, 16
	s_nop 1
	v_writelane_b32 v248, s85, 17
	v_writelane_b32 v248, s82, 30
	s_nop 1
	v_writelane_b32 v248, s83, 31
	s_or_b64 exec, exec, s[0:1]
	s_add_u32 s70, s90, 0x8a7600
	s_addc_u32 s71, s91, 0
	s_add_u32 s0, s90, 0x1e927600
	v_writelane_b32 v248, s0, 24
	s_addc_u32 s0, s91, 0
	v_writelane_b32 v248, s0, 0
	s_add_u32 s0, s90, 0x23367600
	v_writelane_b32 v248, s0, 26
	s_addc_u32 s0, s91, 0
	s_add_u32 s58, s90, 0x25467600
	s_addc_u32 s59, s91, 0
	s_add_u32 s56, s90, 0x2b467600
	s_addc_u32 s57, s91, 0
	v_writelane_b32 v248, s0, 28
	s_add_u32 s0, s90, 0x4700
	s_addc_u32 s1, s91, 0
	s_waitcnt lgkmcnt(0)
	v_mov_b32_e32 v1, v0
	s_barrier
	v_writelane_b32 v248, s0, 13
	s_mul_i32 s3, s33, 3
	v_ashrrev_i32_e32 v1, 8, v1
	v_writelane_b32 v248, s1, 14
	s_mov_b32 s0, 0xd000
	s_lshl_b32 s1, s2, 2
	v_mov_b32_e32 v2, 0xc07c
	s_cmp_ge_u32 s1, s3
	v_mad_i32_i24 v115, v1, s0, v2
	v_mov_b32_e32 v2, 0x6000
	s_cselect_b64 s[74:75], -1, 0
	v_mad_i32_i24 v116, v1, s0, v2
	v_mov_b32_e32 v2, 0xc000
	s_mov_b32 s31, s64
	v_mul_i32_i24_e32 v114, 0xd000, v1
	v_mad_i32_i24 v117, v1, s0, v2
	s_mov_b32 s77, 0
	s_mov_b32 s98, 0
	s_mov_b64 s[54:55], -1
	v_mov_b32_e32 v118, 0x20200
	v_mov_b32_e32 v99, 0
	s_mov_b32 s63, 0x3e38aa3b
	s_mov_b32 s36, 0x3f803f80
	s_mov_b32 s3, 0xc3dc0000
	s_movk_i32 s62, 0x101
	s_mov_b32 s84, 0x20000
	v_mov_b32_e32 v119, 0xffff0000
	v_mov_b32_e32 v120, 0xffff
	v_mov_b32_e32 v121, 0x7b
	v_mov_b32_e32 v122, 0x43dc0000
	v_mov_b32_e32 v123, 0x2000
	v_mov_b32_e32 v124, 0xf149f2ca
	s_mov_b64 s[0:1], s[74:75]
	s_mov_b64 s[86:87], -1
	s_mov_b32 s85, 0
	s_branch .LBB0_373

; __device__ void phase2(const Params& p, unsigned char* smem, unsigned* qw) {
;     ...
;     for (;;) {
;         const bool take_conv = conv_left && (conv_first || !att_left);
;         if (!take_conv && !att_left) break;
;         const int q = (x + aq) & 7;
;         __syncthreads();
;         if (threadIdx.x == 0) *qslot = (int)__hip_atomic_fetch_add(qw + (take_conv ? 0 : 64 * (2 + q)), 1u, __ATOMIC_RELAXED, __HIP_MEMORY_SCOPE_AGENT);
;         __syncthreads();
.LBB0_373:
	s_add_i32 s22, s85, s2
	s_and_b32 s5, s22, 7
	s_barrier
	s_and_saveexec_b64 s[6:7], s[72:73]
	s_cbranch_execz .LBB0_377
	s_mov_b64 s[10:11], exec
	v_mbcnt_lo_u32_b32 v2, s10, 0
	v_mbcnt_hi_u32_b32 v2, s11, v2
	v_cmp_eq_u32_e32 vcc, 0, v2
	s_and_saveexec_b64 s[8:9], vcc
	s_cbranch_execz .LBB0_376
	s_lshl_b32 s4, s5, 6
	s_addk_i32 s4, 0x80
	s_and_b64 s[12:13], s[0:1], exec
	s_cselect_b32 s4, 0, s4
	s_bcnt1_i32_b64 s10, s[10:11]
	s_lshl_b32 s4, s4, 2
	v_mov_b32_e32 v4, s10
	v_readlane_b32 s10, v248, 13
	v_mov_b32_e32 v3, s4
	v_readlane_b32 s11, v248, 14
	s_nop 4
	v_mov_b32_e32 v254, s10
	v_mov_b32_e32 v255, s11
	v_add_co_u32_e32 v254, vcc, v3, v254
	v_addc_co_u32_e32 v255, vcc, 0, v255, vcc
	s_cmp_eq_u32 s98, 1
	s_cbranch_scc1 .Lq_havepf
	global_atomic_add v3, v3, v4, s[10:11] sc0
	s_branch .LBB0_376
.Lq_havepf:
	v_mov_b32_e32 v3, v253

; template <bool ISA>
; __device__ __forceinline__ void attn_unit(const Params& p, unsigned char* smem, int b, int hh, int blk) {
;     ...
;     const int tid = otid() & 255, lane = tid & 63, wid = tid >> 6, l15 = lane & 15, gq = lane >> 4;
;     int nl, tbase;
;     if (ISA) {
;         const int start = blk * 128;
;         const int j0 = start >= 128 ? 0 : 2, j1 = (start + 256 <= SEQ) ? 6 : 4;
;         nl = j1 - j0; tbase = start - 128 + 64 * j0;
;     } else {
;         int rs = 2 * blk - 4; rs = rs < 0 ? 0 : (rs > 119 ? 119 : rs);
;         nl = 9; tbase = rs * 64;
;     }
;     const int ntile = nl + 4;
;     const bf16_t* kbase; const bf16_t* vbase; int ldk;
;     if (ISA) { const int g = hh >> 2; kbase = p.ka + (size_t)(b * TT) * 128 + g * 64; ldk = 128; vbase = p.vta + (size_t)((b * 2 + g) * 64) * TT; }
;     else { kbase = p.kb + (size_t)(b * TT) * 512 + hh * 64; ldk = 512; vbase = p.vtb + (size_t)((b * 8 + hh) * 64) * TT; }
;     float* rpbl = (float*)(smem + 49152);
;     const float M2 = p.attm[ISA ? hh : 8 + hh], negM2 = -M2;
;     const int qt0 = ISA ? blk * 128 + wid * 32 : blk * 128 + wid * 16;
;     bf16x8 qf[NQ][2];
;     {
;         const bf16_t* qsrc = ISA ? p.qa : p.qb;
; #pragma unroll
;         for (int q = 0; q < NQ; ++q)
; #pragma unroll
;             for (int ks = 0; ks < 2; ++ks)
;                 qf[q][ks] = *(const bf16x8*)(qsrc + (size_t)(b * TT + qt0 + q * QSTR + l15) * 512 + hh * 64 + ks * 32 + gq * 8);
;     }
;     f32x4 osum[NQ]; f32x4 o[NQ][4];
; #pragma unroll
;     for (int q = 0; q < NQ; ++q) {
;         const float l0 = ISA ? __builtin_amdgcn_exp2f(p.sink[hh] * L2E - M2) : 0.f;
;         osum[q] = (f32x4){l0, l0, l0, l0};
; #pragma unroll
; __device__ void phase2(const Params& p, unsigned char* smem, unsigned* qw) {
;     ...
;         const int item = *qslot;
;         if (take_conv) {
;             if (item >= nchunks) { conv_left = false; continue; }
;             conv_jobs_deep(p, smem, item * 16, item * 16 + 16);
;         } else {
;             if (item >= 256) { if (++aq == 8) att_left = false; continue; }
;             if (item < 128) {
;                 const int u = item * 2 + sub;
;                 attn_unit<true>(p, sm, q >> 1, (q & 1) * 4 + (u & 3), u >> 2);
;             } else {
;                 const int j = item - 128;
;                 attn_unit<false>(p, sm, j >> 5, q, (j & 31) * 2 + sub);
.LBB0_377:
	s_or_b64 exec, exec, s[6:7]
	s_mov_b32 s98, 0
	s_waitcnt lgkmcnt(0)
	s_barrier
	ds_read_b32 v2, v118
	s_xor_b64 s[6:7], s[0:1], -1
	s_mov_b64 s[0:1], -1
	s_and_b64 vcc, exec, s[6:7]
	s_waitcnt lgkmcnt(0)
	v_readfirstlane_b32 s4, v2
	s_cbranch_vccz .LBB0_429
	s_cmpk_lt_i32 s4, 0x100
	s_cbranch_scc0 .LBB0_426
	s_cmpk_gt_i32 s4, 0x7f
	s_cbranch_scc0 .LBB0_401
	s_add_i32 s0, s4, 0xffffff80
	s_lshr_b32 s24, s0, 5
	s_lshl_b32 s76, s5, 6
	s_lshl_b32 s6, s24, 9
	s_lshl_b32 s0, s4, 1
	s_or_b32 s6, s6, s76
	s_and_b32 s0, s0, 62
	s_mulk_i32 s6, 0x2100
	s_mov_b32 s7, s77
	v_add_u32_e32 v21, s0, v1
	v_mov_b32_e32 v30, v0
	s_lshl_b64 s[6:7], s[6:7], 1
	v_readlane_b32 s9, v248, 26
	v_lshlrev_b32_e32 v101, 1, v21
	v_bfe_u32 v31, v30, 6, 2
	s_add_u32 s6, s9, s6
	v_readlane_b32 s9, v248, 28
	v_add_u32_e32 v19, -4, v101
	s_addc_u32 s7, s9, s7
	s_or_b32 s23, s5, 8
	v_lshlrev_b32_e32 v20, 4, v31
	v_min_i32_e32 v2, 0x77, v19
	s_mul_i32 s8, s24, 0x2100
	s_lshl_b32 s9, s23, 2
	v_lshl_or_b32 v100, v21, 7, v20
	v_lshlrev_b32_e32 v22, 6, v2
	v_mov_b32_e32 v4, s9
	v_add_u32_e32 v2, s8, v100
	s_lshl_b32 s10, s5, 7
	v_readlane_b32 s8, v248, 9
	v_and_b32_e32 v112, 15, v30
	v_readlane_b32 s9, v248, 10
	s_add_u32 s8, s8, s10
	v_or_b32_e32 v6, v2, v112
	s_addc_u32 s9, s9, 0
	v_and_b32_e32 v98, 48, v30
	v_lshl_add_u64 v[8:9], s[8:9], 0, v[98:99]
	v_ashrrev_i32_e32 v7, 31, v6
	v_readlane_b32 s8, v248, 20
	s_mul_i32 s0, s24, 0x420000
	s_mov_b32 s1, s77
	v_lshlrev_b64 v[2:3], 10, v[6:7]
	v_readlane_b32 s9, v248, 21
	v_lshl_add_u64 v[10:11], v[8:9], 0, v[2:3]
	s_nop 3
	global_load_dword v113, v4, s[8:9]
	s_nop 0
	global_load_dwordx4 v[2:5], v[10:11], off
	s_lshl_b64 s[0:1], s[0:1], 1
	v_readlane_b32 s8, v248, 7
	v_readlane_b32 s9, v248, 8
	s_add_u32 s0, s8, s0
	v_cmp_gt_i32_e32 vcc, 2, v21
	v_bfe_u32 v21, v30, 3, 3
	s_addc_u32 s1, s9, s1
	v_or_b32_e32 v21, v20, v21
	v_bfe_u32 v18, v30, 4, 2
	s_add_u32 s0, s0, s10
	v_or_b32_e32 v28, 8, v21
	s_addc_u32 s1, s1, 0
	v_cndmask_b32_e64 v102, v22, 0, vcc
	v_bitop3_b32 v24, v18, v30, 7 bitop3:0x78
	v_lshrrev_b32_e32 v22, 1, v28
	v_lshlrev_b32_e32 v98, 10, v21
	v_xor_b32_e32 v25, v22, v30
	v_lshl_add_u64 v[22:23], s[0:1], 0, v[98:99]
	v_lshlrev_b32_e32 v98, 4, v24
	v_lshl_add_u64 v[104:105], v[22:23], 0, v[98:99]
	v_lshlrev_b32_e32 v22, 10, v28
	v_mov_b32_e32 v23, v99
	v_lshlrev_b32_e32 v24, 4, v25
	v_or_b32_e32 v6, 64, v6
	v_readfirstlane_b32 s8, v31
	v_lshl_add_u64 v[22:23], s[0:1], 0, v[22:23]
	v_and_b32_e32 v24, 0x70, v24
	v_mov_b32_e32 v25, v99
	v_ashrrev_i32_e32 v7, 31, v6
	v_lshl_add_u64 v[106:107], v[22:23], 0, v[24:25]
	v_mov_b64_e32 v[22:23], s[6:7]
	s_movk_i32 s6, 0x4200
	s_lshl_b32 s25, s8, 11
	v_lshlrev_b64 v[6:7], 10, v[6:7]
	v_mad_u64_u32 v[26:27], s[0:1], v21, s6, v[22:23]
	v_mad_u64_u32 v[22:23], s[0:1], v28, s6, v[22:23]
	v_ashrrev_i32_e32 v103, 31, v102
	v_add_u32_e32 v21, s25, v114
	v_lshl_add_u64 v[14:15], v[8:9], 0, v[6:7]
	v_lshl_add_u64 v[108:109], v[26:27], 0, v[98:99]
	v_lshl_add_u64 v[110:111], v[22:23], 0, v[24:25]
	v_lshlrev_b64 v[22:23], 10, v[102:103]
	v_readfirstlane_b32 s0, v21
	v_add_u32_e32 v26, 0x400, v21
	global_load_dwordx4 v[6:9], v[10:11], off offset:64
	s_nop 0
	global_load_dwordx4 v[10:13], v[14:15], off
	s_nop 0
	global_load_dwordx4 v[14:17], v[14:15], off offset:64
	s_waitcnt lgkmcnt(0)
	s_barrier
; #define LAS __attribute__((address_space(3)))
; template <bool ISA>
; __device__ __forceinline__ void attn_unit(const Params& p, unsigned char* smem, int b, int hh, int blk) {
;     ...
;     const int qcol = wid * 16 + l15;
;     int cs = wid * 16 - 8; cs = cs < 0 ? 0 : (cs > 32 ? 32 : cs);
;     int wstart = qcol - 8; wstart = wstart < 0 ? 0 : (wstart > 48 ? 48 : wstart);
;     NaConst nc;
; #pragma unroll
;     for (int j = 0; j < 4; ++j) {
;         const int kc = cs + (j >> 1) * 16 + gq * 4 + (j & 1) * 2;
;         nc.cm[j] = (((kc >= wstart) && (kc < wstart + 16)) ? 0xFFFFu : 0u) | (((kc + 1 >= wstart) && (kc + 1 < wstart + 16)) ? 0xFFFF0000u : 0u);
;     }
;     nc.blane = (unsigned)(size_t)(LAS unsigned char*)smem + 49152u + (unsigned)((16 + (cs + gq * 4 - qcol + 15)) * 4);
;     LAS unsigned char* ldsu = (LAS unsigned char*)smem;
;     const unsigned ldsa = (unsigned)(size_t)ldsu;
;     const int wuni = __builtin_amdgcn_readfirstlane(wid);
;     const bf16_t* kp0; const bf16_t* kp1; const bf16_t* vp0; const bf16_t* vp1;
;     {
;         const int ra = (wid * 2) * 8 + (lane >> 3), rb = (wid * 2 + 1) * 8 + (lane >> 3);
;         const int ca = ((lane & 7) ^ ((ra >> 1) & 7)) * 8, cb = ((lane & 7) ^ ((rb >> 1) & 7)) * 8;
;         kp0 = kbase + (size_t)ra * ldk + ca; kp1 = kbase + (size_t)rb * ldk + cb;
;         vp0 = vbase + (size_t)ra * TT + ca; vp1 = vbase + (size_t)rb * TT + cb;
;     }
;     ...
;     asm volatile("s_waitcnt lgkmcnt(0)" ::: "memory"); __builtin_amdgcn_s_barrier(); asm volatile("" ::: "memory");
;     ADMA(0);
;     if (ntile > 1) ADMA(1);
;     if (!ISA) {
;         for (int i = tid; i < 15 * 64; i += 256) { const int dr = i >> 6, dc = (i & 63) - 16; rpbl[i] = ((dc >= 0 && dc < 31) ? p.rpb[hh * 465 + dr * 31 + dc] * L2E : 0.f) - M2; }
	v_lshl_add_u64 v[24:25], v[104:105], 0, v[22:23]
	s_mov_b32 m0, s0
	v_readfirstlane_b32 s0, v26
	global_load_lds_dwordx4 v[24:25], off
	v_lshl_add_u64 v[24:25], v[106:107], 0, v[22:23]
	s_mov_b32 m0, s0
	v_add_u32_e32 v28, 0x6000, v21
	global_load_lds_dwordx4 v[24:25], off
	v_lshlrev_b64 v[24:25], 1, v[102:103]
	v_readfirstlane_b32 s0, v28
	v_add_u32_e32 v28, 0x6400, v21
	v_lshl_add_u64 v[26:27], v[108:109], 0, v[24:25]
	s_mov_b32 m0, s0
	v_readfirstlane_b32 s0, v28
	global_load_lds_dwordx4 v[26:27], off
	s_mov_b32 m0, s0
	s_mov_b64 s[0:1], 0x10000
	v_add_u32_e32 v32, 0x2000, v21
	v_lshl_add_u64 v[24:25], v[110:111], 0, v[24:25]
	v_lshl_add_u64 v[22:23], v[22:23], 0, s[0:1]
	v_readfirstlane_b32 s0, v32
	global_load_lds_dwordx4 v[24:25], off
	v_lshl_add_u64 v[28:29], v[104:105], 0, v[22:23]
	s_mov_b32 m0, s0
	v_lshl_add_u64 v[22:23], v[106:107], 0, v[22:23]
	global_load_lds_dwordx4 v[28:29], off
	v_add_u32_e32 v28, 0x2400, v21
	s_mov_b64 s[6:7], 0x80
	v_readfirstlane_b32 s0, v28
	s_mov_b32 m0, s0
	v_and_b32_e32 v103, 63, v30
	global_load_lds_dwordx4 v[22:23], off
	v_lshl_add_u64 v[22:23], v[26:27], 0, s[6:7]
	v_add_u32_e32 v26, 0x8000, v21
	v_add_u32_e32 v21, 0x8400, v21
	v_readfirstlane_b32 s0, v26
	s_mov_b32 m0, s0
	v_readfirstlane_b32 s0, v21
	global_load_lds_dwordx4 v[22:23], off
	v_lshl_add_u64 v[22:23], v[24:25], 0, s[6:7]
	s_mov_b32 m0, s0
	s_mul_i32 s6, s5, 0x1d1
	global_load_lds_dwordx4 v[22:23], off
	v_and_b32_e32 v23, 0xff, v30
	v_add_u32_e32 v22, -16, v103
	s_add_i32 s6, s6, -16
	v_mul_u32_u24_e32 v24, 31, v31
	v_lshlrev_b32_e32 v21, 3, v18
	v_cmp_gt_u32_e64 s[0:1], 31, v22
	v_lshl_add_u32 v22, v23, 2, v117
	v_add3_u32 v98, s6, v24, v103
	v_or_b32_e32 v23, 0xffffff00, v23
	v_mov_b32_e32 v26, 0
	v_mov_b32_e32 v27, 0
	v_mov_b32_e32 v28, 0
	v_mov_b32_e32 v29, 0
	v_and_b32_e32 v32, 0xff, v30
	s_movk_i32 s8, 0xc0
	v_lshl_add_u64 v[24:25], v[98:99], 2, s[80:81]
	v_cmp_gt_u32_e64 s[8:9], s8, v32
	s_and_saveexec_b64 s[6:7], s[0:1]
	global_load_dword v26, v[24:25], off
	global_load_dword v27, v[24:25], off offset:496
	global_load_dword v28, v[24:25], off offset:992
	s_and_b64 exec, exec, s[8:9]
	global_load_dword v29, v[24:25], off offset:1488
	s_mov_b64 exec, s[6:7]
	s_waitcnt vmcnt(0)
	v_mul_f32_e32 v26, 0x3fb8aa3b, v26
	v_mul_f32_e32 v27, 0x3fb8aa3b, v27
	v_mul_f32_e32 v28, 0x3fb8aa3b, v28
	v_mul_f32_e32 v29, 0x3fb8aa3b, v29
	v_sub_f32_e32 v26, v26, v113
	v_sub_f32_e32 v27, v27, v113
	v_sub_f32_e32 v28, v28, v113
	v_sub_f32_e32 v29, v29, v113
	ds_write_b32 v22, v26
	ds_write_b32 v22, v27 offset:1024
	ds_write_b32 v22, v28 offset:2048
	s_and_saveexec_b64 s[6:7], s[8:9]
	ds_write_b32 v22, v29 offset:3072
	s_or_b64 exec, exec, s[6:7]
	v_or_b32_e32 v22, v20, v112
	v_med3_u32 v20, v20, 8, 40
	v_add_u32_e32 v20, -8, v20
	v_med3_u32 v23, v22, 8, 56
	v_lshlrev_b32_e32 v98, 2, v18
	v_add_u32_e32 v24, v20, v98
	v_add_u32_e32 v25, 8, v23
	v_add_u32_e32 v23, -8, v23
	v_cmp_lt_u32_e64 s[0:1], v24, v25
	v_or_b32_e32 v26, 1, v24
	v_cmp_ge_u32_e64 s[20:21], v24, v23
	v_cmp_lt_u32_e64 s[6:7], v26, v25
	v_add_u32_e32 v29, 16, v24
	s_and_b64 s[0:1], s[20:21], s[0:1]
	v_cmp_ge_u32_e64 s[20:21], v26, v23
	v_or_b32_e32 v27, 2, v24
	v_or_b32_e32 v28, 3, v24
	v_add_u32_e32 v30, 17, v24
	v_or_b32_e32 v31, 2, v29
	v_add_u32_e32 v32, 19, v24
	s_and_b64 s[6:7], s[20:21], s[6:7]
	v_cmp_lt_u32_e64 s[8:9], v27, v25
	v_cmp_lt_u32_e64 s[10:11], v28, v25
	v_cmp_lt_u32_e64 s[12:13], v29, v25
	v_cmp_lt_u32_e64 s[14:15], v30, v25
	v_cmp_lt_u32_e64 s[16:17], v31, v25
	v_cmp_lt_u32_e64 s[18:19], v32, v25
	v_cndmask_b32_e64 v25, 0, v119, s[6:7]
	v_cmp_ge_u32_e64 s[6:7], v27, v23
	s_and_b64 s[6:7], s[6:7], s[8:9]
	v_cmp_ge_u32_e64 s[8:9], v28, v23
	s_and_b64 s[8:9], s[8:9], s[10:11]
	v_cmp_ge_u32_e64 s[10:11], v30, v23
	v_cndmask_b32_e64 v26, 0, v119, s[8:9]
	v_cmp_ge_u32_e64 s[8:9], v29, v23
	s_and_b64 s[10:11], s[10:11], s[14:15]
	v_cndmask_b32_e64 v28, 0, v120, s[0:1]
	s_and_b64 s[8:9], s[8:9], s[12:13]
	v_cndmask_b32_e64 v27, 0, v119, s[10:11]
	v_cmp_ge_u32_e64 s[10:11], v31, v23
	v_cmp_ge_u32_e64 s[12:13], v32, v23
	v_or_b32_e32 v125, v25, v28
	v_cndmask_b32_e64 v25, 0, v120, s[6:7]
	v_sub_u32_e32 v22, v24, v22
	s_and_b64 s[10:11], s[10:11], s[16:17]
	s_and_b64 s[12:13], s[12:13], s[18:19]
	v_or_b32_e32 v126, v26, v25
	v_cndmask_b32_e64 v25, 0, v120, s[8:9]
	v_min_i32_e32 v19, 0x78, v19
	v_cndmask_b32_e64 v23, 0, v119, s[12:13]
	v_or_b32_e32 v127, v27, v25
	v_cndmask_b32_e64 v25, 0, v120, s[10:11]
	v_lshl_add_u32 v129, v22, 2, v115
	v_lshrrev_b32_e32 v22, 1, v112
	v_cndmask_b32_e64 v137, v19, 0, vcc
	v_med3_i32 v19, v101, 3, v121
	v_or_b32_e32 v128, v25, v23
	v_xor_b32_e32 v25, v18, v22
	v_add_u32_e32 v138, -3, v19
	v_add_u32_e32 v140, 5, v19
	v_add_u16_e32 v19, v20, v112
	v_lshlrev_b32_e32 v131, 4, v25
	v_bitop3_b32 v25, v18, v22, 4 bitop3:0x36
	v_lshrrev_b16_e32 v19, 1, v19
	v_or_b32_e32 v23, 4, v18
	v_lshlrev_b32_e32 v132, 4, v25
	v_lshrrev_b32_e32 v25, 5, v103
	v_bitop3_b32 v18, v19, v18, 7 bitop3:0x6c
	v_xor_b32_e32 v26, v25, v22
	v_lshlrev_b32_e32 v142, 4, v18
	v_bitop3_b32 v18, v19, v23, 7 bitop3:0x6c
	v_lshlrev_b32_e32 v130, 7, v112
	v_and_b32_e32 v21, 8, v21
	v_lshlrev_b32_e32 v26, 4, v26
	v_lshlrev_b32_e32 v143, 4, v18
	v_lshrrev_b32_e32 v18, 3, v24
	v_or3_b32 v134, v26, v130, v21
	v_bitop3_b32 v26, v25, v22, 2 bitop3:0x36
	v_xor_b32_e32 v18, v18, v22
	v_lshlrev_b32_e32 v135, 4, v26
	v_bitop3_b32 v26, v25, v22, 4 bitop3:0x36
	v_lshlrev_b32_e32 v144, 4, v18
	v_lshlrev_b32_e32 v18, 1, v24
	v_lshlrev_b32_e32 v26, 4, v26
	v_and_or_b32 v145, v18, 8, v130
	v_lshrrev_b32_e32 v18, 3, v29
	v_or_b32_e32 v133, v21, v130
	v_bitop3_b32 v25, v25, v22, 6 bitop3:0x36
	v_add_lshl_u32 v141, v20, v112, 7
	v_xor_b32_e32 v18, v18, v22
	v_or3_b32 v147, v130, v26, v21
	v_mov_b32_e32 v20, v99
	v_mov_b32_e32 v21, v99
	v_lshlrev_b32_e32 v136, 4, v25
	v_lshlrev_b32_e32 v146, 4, v18
	v_mov_b32_e32 v18, v99
	v_mov_b32_e32 v19, v99
	v_mov_b32_e32 v50, 0
	v_mov_b64_e32 v[24:25], v[20:21]
	v_mov_b64_e32 v[28:29], v[20:21]
	v_mov_b64_e32 v[32:33], v[20:21]
	v_mov_b64_e32 v[36:37], v[20:21]
	v_mov_b64_e32 v[40:41], v[20:21]
	v_mov_b64_e32 v[44:45], v[20:21]
	v_mov_b64_e32 v[48:49], v[20:21]
	s_mov_b32 s26, 2
	v_add_u32_e32 v139, 8, v137
	s_movk_i32 s8, 0x1e40
	v_mov_b64_e32 v[22:23], v[18:19]
	v_mov_b64_e32 v[26:27], v[18:19]
	v_mov_b64_e32 v[30:31], v[18:19]
	v_mov_b64_e32 v[34:35], v[18:19]
	v_mov_b64_e32 v[38:39], v[18:19]
	v_mov_b64_e32 v[42:43], v[18:19]
	v_mov_b64_e32 v[46:47], v[18:19]
	v_mov_b32_e32 v51, v50
	v_mov_b32_e32 v52, v50
	v_mov_b32_e32 v53, v50
	v_mov_b32_e32 v54, v50
	v_mov_b32_e32 v55, v50
	v_mov_b32_e32 v56, v50
	v_mov_b32_e32 v57, v50
	s_cmpk_eq_i32 s8, 0x2140
	s_mov_b64 s[0:1], -1
	s_cbranch_scc1 .LBB0_386

; template <bool ISA>
; __device__ __forceinline__ void attn_unit(const Params& p, unsigned char* smem, int b, int hh, int blk) {
;     ...
; #pragma unroll
;     for (int q = 0; q < NQ; ++q) {
;         const float inv = 1.0f / osum[q][0];
;         float ssq = 0.f;
; #pragma unroll
;         for (int df = 0; df < 4; ++df) { o[q][df] *= inv; ssq += o[q][df][0] * o[q][df][0] + o[q][df][1] * o[q][df][1] + o[q][df][2] * o[q][df][2] + o[q][df][3] * o[q][df][3]; }
;         ssq += __shfl_xor(ssq, 16); ssq += __shfl_xor(ssq, 32);
;         const size_t lr = (size_t)b * SEQ + qt0 + q * QSTR + l15;
;         if (gq == 0) p.osq[lr * 16 + (ISA ? hh : 8 + hh)] = ssq;
; __device__ void phase2(const Params& p, unsigned char* smem, unsigned* qw) {
;     ...
;         if (threadIdx.x == 0) *qslot = (int)__hip_atomic_fetch_add(qw + (take_conv ? 0 : 64 * (2 + q)), 1u, __ATOMIC_RELAXED, __HIP_MEMORY_SCOPE_AGENT);
.LBB0_396:
	s_mov_b32 s98, 1
	v_cmp_eq_u32_e32 vcc, 0, v0
	s_and_saveexec_b64 s[100:101], vcc
	s_cbranch_execz .Lq3_xb
	v_mov_b32_e32 v252, 1
	global_atomic_add v253, v[254:255], v252, off sc0
.Lq3_xb:
	s_mov_b64 exec, s[100:101]
	v_and_b32_e32 v3, 64, v214
	v_add_u32_e32 v5, 64, v3
	v_div_scale_f32 v3, s[0:1], v78, v78, 1.0
	v_rcp_f32_e32 v4, v3
	v_xor_b32_e32 v2, 16, v214
	v_cmp_lt_i32_e32 vcc, v2, v5
	v_xor_b32_e32 v20, 32, v214
	s_lshl_b32 s0, s24, 13
	v_cndmask_b32_e32 v2, v214, v2, vcc
	v_lshlrev_b32_e32 v22, 2, v2
	v_fma_f32 v2, -v3, v4, 1.0
	v_fmac_f32_e32 v4, v2, v4
	v_div_scale_f32 v2, vcc, 1.0, v78, 1.0
	v_mul_f32_e32 v6, v2, v4
	v_fma_f32 v7, -v3, v6, v2
	v_fmac_f32_e32 v6, v7, v4
	v_fma_f32 v2, -v3, v6, v2
	v_div_fmas_f32 v2, v2, v4, v6
	v_div_fixup_f32 v4, v2, v78, 1.0
	v_pk_mul_f32 v[18:19], v[82:83], v[4:5] op_sel_hi:[1,0]
	v_pk_mul_f32 v[16:17], v[86:87], v[4:5] op_sel_hi:[1,0]
	v_mul_f32_e32 v2, v19, v19
	v_mul_f32_e32 v3, v17, v17
	v_pk_mul_f32 v[14:15], v[84:85], v[4:5] op_sel_hi:[1,0]
	v_fmac_f32_e32 v2, v18, v18
	v_pk_mul_f32 v[8:9], v[88:89], v[4:5] op_sel_hi:[1,0]
	v_fmac_f32_e32 v3, v16, v16
	v_fmac_f32_e32 v2, v14, v14
	v_fmac_f32_e32 v3, v8, v8
	v_fmac_f32_e32 v2, v15, v15
	v_fmac_f32_e32 v3, v9, v9
	v_pk_mul_f32 v[12:13], v[90:91], v[4:5] op_sel_hi:[1,0]
	v_add_f32_e32 v2, v2, v3
	v_mul_f32_e32 v3, v13, v13
	v_pk_mul_f32 v[6:7], v[92:93], v[4:5] op_sel_hi:[1,0]
	v_fmac_f32_e32 v3, v12, v12
	v_fmac_f32_e32 v3, v6, v6
	v_fmac_f32_e32 v3, v7, v7
	v_pk_mul_f32 v[10:11], v[94:95], v[4:5] op_sel_hi:[1,0]
	v_add_f32_e32 v21, v3, v2
	v_pk_mul_f32 v[2:3], v[96:97], v[4:5] op_sel_hi:[1,0]
	v_mul_f32_e32 v4, v11, v11
	v_fmac_f32_e32 v4, v10, v10
	v_fmac_f32_e32 v4, v2, v2
	v_fmac_f32_e32 v4, v3, v3
	v_add_f32_e32 v4, v4, v21
	ds_bpermute_b32 v21, v22, v4
	v_cmp_lt_i32_e32 vcc, v20, v5
	s_mov_b32 s1, s77
	v_ashrrev_i32_e32 v101, 31, v100
	v_cndmask_b32_e32 v5, v214, v20, vcc
	v_lshlrev_b32_e32 v23, 2, v5
	s_waitcnt lgkmcnt(0)
	v_add_f32_e32 v20, v4, v21
	ds_bpermute_b32 v21, v23, v20
	v_lshl_add_u64 v[4:5], v[100:101], 0, s[0:1]
	v_or_b32_e32 v4, v4, v112
	v_cmp_gt_u32_e64 s[0:1], 16, v103
	s_and_saveexec_b64 s[6:7], s[0:1]
	s_cbranch_execz .LBB0_398
	s_waitcnt lgkmcnt(0)
	v_add_f32_e32 v24, v20, v21
	v_lshlrev_b64 v[20:21], 6, v[4:5]
	v_lshl_add_u64 v[20:21], s[70:71], 0, v[20:21]
	s_lshl_b32 s8, s23, 2
	s_mov_b32 s9, s77
	v_lshl_add_u64 v[20:21], v[20:21], 0, s[8:9]
	global_store_dword v[20:21], v24, off

; template <bool ISA>
; __device__ __forceinline__ void attn_unit(const Params& p, unsigned char* smem, int b, int hh, int blk) {
;     ...
; #pragma unroll
;     for (int q = 0; q < NQ; ++q) {
;         const float inv = 1.0f / osum[q][0];
;         float ssq = 0.f;
; #pragma unroll
;         for (int df = 0; df < 4; ++df) { o[q][df] *= inv; ssq += o[q][df][0] * o[q][df][0] + o[q][df][1] * o[q][df][1] + o[q][df][2] * o[q][df][2] + o[q][df][3] * o[q][df][3]; }
;         ssq += __shfl_xor(ssq, 16); ssq += __shfl_xor(ssq, 32);
;         const size_t lr = (size_t)b * SEQ + qt0 + q * QSTR + l15;
;         if (gq == 0) p.osq[lr * 16 + (ISA ? hh : 8 + hh)] = ssq;
; __device__ void phase2(const Params& p, unsigned char* smem, unsigned* qw) {
;     ...
;         if (threadIdx.x == 0) *qslot = (int)__hip_atomic_fetch_add(qw + (take_conv ? 0 : 64 * (2 + q)), 1u, __ATOMIC_RELAXED, __HIP_MEMORY_SCOPE_AGENT);
.LBB0_420:
	s_or_b64 exec, exec, s[82:83]
	s_mov_b32 s98, 1
	v_cmp_eq_u32_e32 vcc, 0, v0
	s_and_saveexec_b64 s[100:101], vcc
	s_cbranch_execz .Lq3_xa
	v_mov_b32_e32 v252, 1
	global_atomic_add v253, v[254:255], v252, off sc0
.Lq3_xa:
	s_mov_b64 exec, s[100:101]
	v_and_b32_e32 v3, 64, v214
	v_xor_b32_e32 v2, 16, v214
	v_add_u32_e32 v3, 64, v3
	v_cmp_lt_i32_e32 vcc, v2, v3
	v_div_scale_f32 v4, s[0:1], v38, v38, 1.0
	s_nop 0
	v_cndmask_b32_e32 v2, v214, v2, vcc
	v_rcp_f32_e32 v5, v4
	v_lshlrev_b32_e32 v40, 2, v2
	v_xor_b32_e32 v2, 32, v214
	v_cmp_lt_i32_e32 vcc, v2, v3
	s_lshl_b32 s76, s5, 13
	v_ashrrev_i32_e32 v85, 31, v84
	v_cndmask_b32_e32 v2, v214, v2, vcc
	v_lshlrev_b32_e32 v41, 2, v2
	v_fma_f32 v2, -v4, v5, 1.0
	v_fmac_f32_e32 v5, v2, v5
	v_div_scale_f32 v2, vcc, 1.0, v38, 1.0
	v_mul_f32_e32 v3, v2, v5
	v_fma_f32 v6, -v4, v3, v2
	v_fmac_f32_e32 v3, v6, v5
	v_fma_f32 v2, -v4, v3, v2
	v_div_fmas_f32 v2, v2, v5, v3
	v_div_fixup_f32 v2, v2, v38, 1.0
	v_pk_mul_f32 v[38:39], v[66:67], v[2:3] op_sel_hi:[1,0]
	v_pk_mul_f32 v[8:9], v[68:69], v[2:3] op_sel_hi:[1,0]
	v_mul_f32_e32 v3, v39, v39
	v_fmac_f32_e32 v3, v38, v38
	v_fmac_f32_e32 v3, v8, v8
	v_fmac_f32_e32 v3, v9, v9
	v_pk_mul_f32 v[28:29], v[62:63], v[2:3] op_sel_hi:[1,0]
	v_pk_mul_f32 v[12:13], v[64:65], v[2:3] op_sel_hi:[1,0]
	v_mul_f32_e32 v4, v29, v29
	v_fmac_f32_e32 v4, v28, v28
	v_fmac_f32_e32 v4, v12, v12
	v_fmac_f32_e32 v4, v13, v13
	v_add_f32_e32 v3, v3, v4
	v_pk_mul_f32 v[16:17], v[42:43], v[2:3] op_sel_hi:[1,0]
	v_pk_mul_f32 v[10:11], v[44:45], v[2:3] op_sel_hi:[1,0]
	v_mul_f32_e32 v4, v17, v17
	v_fmac_f32_e32 v4, v16, v16
	v_fmac_f32_e32 v4, v10, v10
	v_fmac_f32_e32 v4, v11, v11
	v_add_f32_e32 v3, v4, v3
	v_pk_mul_f32 v[14:15], v[34:35], v[2:3] op_sel_hi:[1,0]
	v_pk_mul_f32 v[6:7], v[36:37], v[2:3] op_sel_hi:[1,0]
	v_mul_f32_e32 v2, v15, v15
	v_fmac_f32_e32 v2, v14, v14
	v_fmac_f32_e32 v2, v6, v6
	v_fmac_f32_e32 v2, v7, v7
	v_add_f32_e32 v4, v2, v3
	ds_bpermute_b32 v5, v40, v4
	v_lshl_add_u64 v[2:3], v[84:85], 0, s[76:77]
	v_or_b32_e32 v2, v2, v83
	v_cmp_gt_u32_e64 s[0:1], 16, v87
	s_waitcnt lgkmcnt(0)
	v_add_f32_e32 v27, v4, v5
	ds_bpermute_b32 v34, v41, v27
	v_lshlrev_b32_e32 v4, 2, v82
	v_mov_b32_e32 v5, v99
	v_lshl_add_u64 v[4:5], s[70:71], 0, v[4:5]
	s_and_saveexec_b64 s[6:7], s[0:1]
	s_cbranch_execz .LBB0_422
	s_waitcnt lgkmcnt(0)
	v_add_f32_e32 v27, v27, v34
	v_lshlrev_b64 v[34:35], 6, v[2:3]
	v_lshl_add_u64 v[34:35], v[4:5], 0, v[34:35]
	global_store_dword v[34:35], v27, off
